# split-phase SEAM(9): the conversion workgroups (F.loc, rank>=16) arrive at the grid barrier but do not wait for its release before starting their P10 weight conversions
# speedup vs baseline: 1.0058x; 1.0058x over previous
; #define SEAM(k) do { if (IN(k) && IN((k) + 1)) xcd_barrier(bar, F.wave == 0 && pg8::pg8_lane_id() == 0); } while (0)
; __device__ __forceinline__ void xcd_barrier(const XcdBarrier& b, const bool xb_leader) {
;     asm volatile("s_waitcnt vmcnt(0)" ::: "memory");
;     __syncthreads();
;     if (xb_leader) {
;         unsigned* bar = b.bar;
;         __builtin_amdgcn_s_waitcnt(0);
;         unsigned nloc = b.st[0], nx = b.st[1];
;         if (nloc == 0u) { unsigned bal; xcd_barrier_complete(bar, b.x, nloc, nx, bal); b.st[0] = nloc; b.st[1] = nx; b.st[3] = bal; }
; __global__ void __launch_bounds__(NWAVES * 64, 2) mk_fwd(Args args) {
;     ...
;     } SEAM(9);
.LBB0_1188:
	s_waitcnt vmcnt(0)
	s_waitcnt vmcnt(0) lgkmcnt(0)
	s_barrier
	s_and_saveexec_b64 s[0:1], s[6:7]
	s_cbranch_execz .LBB0_1247
	s_cmpk_eq_i32 s33, 0x100
	s_cselect_b64 s[98:99], -1, 0
	s_cmp_gt_i32 s2, 127
	s_cselect_b64 s[100:101], -1, 0
	s_and_b64 s[98:99], s[98:99], s[100:101]
	v_readlane_b32 s100, v254, 24
	v_readlane_b32 s101, v254, 25
	s_and_b64 s[98:99], s[98:99], s[100:101]
	s_add_i32 s3, 0, 0x20160
	v_mov_b32_e32 v0, s3
	s_waitcnt vmcnt(0) expcnt(0) lgkmcnt(0)
	buffer_inv sc1
	ds_read_b32 v9, v0
	s_add_i32 s3, 0, 0x20164
	v_mov_b32_e32 v0, s3
	ds_read_b32 v8, v0
	s_waitcnt lgkmcnt(1)
	v_cmp_ne_u32_e32 vcc, 0, v9
	s_cbranch_vccnz .LBB0_1211
	v_readlane_b32 s6, v254, 0
	v_readlane_b32 s7, v254, 1
	s_load_dwordx2 s[10:11], s[6:7], 0x4
	s_add_u32 s6, s28, 0x1000
	s_addc_u32 s7, s29, 0
	s_add_u32 s8, s28, 0x1100
	s_addc_u32 s9, s29, 0
	s_waitcnt lgkmcnt(0)
	s_mul_i32 s3, s10, s33
	s_add_u32 s10, s28, 0x1200
	s_mul_i32 s3, s3, s11
	s_addc_u32 s11, s29, 0
	s_add_u32 s12, s28, 0x1300
	s_addc_u32 s13, s29, 0
	s_mov_b32 s44, 1
	v_mov_b32_e32 v8, 0
	s_branch .LBB0_1193

; __device__ __forceinline__ unsigned xb_ld(unsigned* p)              { return __hip_atomic_load(p, __ATOMIC_RELAXED, __HIP_MEMORY_SCOPE_AGENT); }
; __device__ __forceinline__ unsigned xb_add(unsigned* p, unsigned v) { return __hip_atomic_fetch_add(p, v, __ATOMIC_RELAXED, __HIP_MEMORY_SCOPE_AGENT); }
; #define XB_SPIN(cond, bar) do { unsigned _sp = 0; while (cond) { __builtin_amdgcn_s_sleep(1); \
;     if ((++_sp & 255u) == 0u) { if (xb_ld(&(bar)[XB_TMO])) break; if (_sp > XB_SPIN_CAP) { atomicAdd(&(bar)[XB_TMO], 1u); break; } } } } while (0)
; __device__ __forceinline__ void xcd_barrier(const XcdBarrier& b, const bool xb_leader) {
;     ...
;         const unsigned old = xb_add(&bar[XB_XSUB(b.x)], 1u);
;         const unsigned gen = old / nloc;
;         if (old + 1u == (gen + 1u) * nloc) {
;             __builtin_amdgcn_fence(__ATOMIC_RELEASE, "agent");
;             asm volatile("s_waitcnt vmcnt(0)" ::: "memory");
;             const unsigned og = xb_add(&bar[XB_TOP], 1u);
;             const unsigned tg = og / nx;
;             if (og + 1u == (tg + 1u) * nx) xb_add(&bar[XB_TOPGEN], 1u);
;             else XB_SPIN(xb_ld(&bar[XB_TOPGEN]) == tg, bar);
;             __builtin_amdgcn_fence(__ATOMIC_ACQUIRE, "agent");
;             xb_add(&bar[XB_XGEN(b.x)], 1u);
;             asm volatile("s_waitcnt vmcnt(0)" ::: "memory");
;         } else {
;             XB_SPIN(xb_ld(&bar[XB_XGEN(b.x)]) == gen, bar);
.LBB0_1213:
	s_or_b64 exec, exec, s[10:11]
	v_cvt_f32_u32_e32 v2, v9
	s_waitcnt vmcnt(0)
	v_readfirstlane_b32 s3, v1
	v_sub_u32_e32 v1, 0, v9
	v_rcp_iflag_f32_e32 v2, v2
	v_add_u32_e32 v3, s3, v0
	v_mul_f32_e32 v2, 0x4f7ffffe, v2
	v_cvt_u32_f32_e32 v2, v2
	v_mul_lo_u32 v0, v1, v2
	v_mul_hi_u32 v0, v2, v0
	v_add_u32_e32 v0, v2, v0
	v_mul_hi_u32 v0, v3, v0
	v_mul_lo_u32 v1, v0, v9
	v_sub_u32_e32 v1, v3, v1
	v_add_u32_e32 v2, 1, v0
	v_cmp_ge_u32_e32 vcc, v1, v9
	s_nop 1
	v_cndmask_b32_e32 v0, v0, v2, vcc
	v_sub_u32_e32 v2, v1, v9
	v_cndmask_b32_e32 v1, v1, v2, vcc
	v_add_u32_e32 v2, 1, v0
	v_cmp_ge_u32_e32 vcc, v1, v9
	v_add_u32_e32 v1, 1, v3
	s_nop 0
	v_cndmask_b32_e32 v0, v0, v2, vcc
	v_mul_lo_u32 v2, v9, v0
	v_add_u32_e32 v2, v2, v9
	v_cmp_ne_u32_e32 vcc, v1, v2
	s_and_saveexec_b64 s[8:9], vcc
	s_xor_b64 s[8:9], exec, s[8:9]
	s_cbranch_execz .LBB0_1227
	s_waitcnt lgkmcnt(0)
	v_add_u32_e32 v0, 1, v0
	v_mul_lo_u32 v0, v0, v8
	v_mov_b32_e32 v1, 0x3000
	global_load_dword v1, v1, s[28:29] offset:1024 sc1
	s_add_u32 s12, s28, 0x3400
	s_addc_u32 s13, s29, 0
	s_waitcnt vmcnt(0)
	v_cmp_lt_u32_e32 vcc, v1, v0
	s_andn2_b64 vcc, vcc, s[98:99]
	s_and_saveexec_b64 s[10:11], vcc
	s_cbranch_execz .LBB0_1226
	s_mov_b32 s3, 1
	s_mov_b64 s[14:15], 0
	v_mov_b32_e32 v1, 0
	s_branch .LBB0_1217

; __device__ __forceinline__ unsigned xb_ld(unsigned* p)              { return __hip_atomic_load(p, __ATOMIC_RELAXED, __HIP_MEMORY_SCOPE_AGENT); }
; __device__ __forceinline__ unsigned xb_add(unsigned* p, unsigned v) { return __hip_atomic_fetch_add(p, v, __ATOMIC_RELAXED, __HIP_MEMORY_SCOPE_AGENT); }
; #define XB_SPIN(cond, bar) do { unsigned _sp = 0; while (cond) { __builtin_amdgcn_s_sleep(1); \
;     if ((++_sp & 255u) == 0u) { if (xb_ld(&(bar)[XB_TMO])) break; if (_sp > XB_SPIN_CAP) { atomicAdd(&(bar)[XB_TMO], 1u); break; } } } } while (0)
; __device__ __forceinline__ void xcd_barrier(const XcdBarrier& b, const bool xb_leader) {
;     ...
;         const unsigned old = xb_add(&bar[XB_XSUB(b.x)], 1u);
;         const unsigned gen = old / nloc;
;         if (old + 1u == (gen + 1u) * nloc) {
;             __builtin_amdgcn_fence(__ATOMIC_RELEASE, "agent");
;             asm volatile("s_waitcnt vmcnt(0)" ::: "memory");
;             const unsigned og = xb_add(&bar[XB_TOP], 1u);
;             const unsigned tg = og / nx;
;             if (og + 1u == (tg + 1u) * nx) xb_add(&bar[XB_TOPGEN], 1u);
;             else XB_SPIN(xb_ld(&bar[XB_TOPGEN]) == tg, bar);
.LBB0_1230:
	s_or_b64 exec, exec, s[10:11]
	v_cvt_f32_u32_e32 v2, v8
	s_waitcnt vmcnt(0)
	v_readfirstlane_b32 s3, v1
	s_add_u32 s10, s28, 0x3400
	s_addc_u32 s11, s29, 0
	v_rcp_iflag_f32_e32 v2, v2
	v_add_u32_e32 v0, s3, v0
	v_add_u32_e32 v3, 1, v0
	s_mov_b64 s[12:13], 0
	v_mul_f32_e32 v1, 0x4f7ffffe, v2
	v_cvt_u32_f32_e32 v1, v1
	v_sub_u32_e32 v2, 0, v8
	v_mul_lo_u32 v2, v2, v1
	v_mul_hi_u32 v2, v1, v2
	v_add_u32_e32 v1, v1, v2
	v_mul_hi_u32 v1, v0, v1
	v_mul_lo_u32 v2, v1, v8
	v_sub_u32_e32 v0, v0, v2
	v_add_u32_e32 v4, 1, v1
	v_cmp_ge_u32_e32 vcc, v0, v8
	v_sub_u32_e32 v2, v0, v8
	s_nop 0
	v_cndmask_b32_e32 v1, v1, v4, vcc
	v_cndmask_b32_e32 v0, v0, v2, vcc
	v_add_u32_e32 v2, 1, v1
	v_cmp_ge_u32_e32 vcc, v0, v8
	s_nop 1
	v_cndmask_b32_e32 v2, v1, v2, vcc
	v_mul_lo_u32 v0, v8, v2
	v_add_u32_e32 v0, v0, v8
	v_cmp_ne_u32_e32 vcc, v3, v0
	v_mov_b32_e32 v4, v0
	v_mov_b64_e32 v[0:1], s[10:11]
	s_and_saveexec_b64 s[8:9], vcc
	s_cbranch_execz .LBB0_1242
	v_mov_b32_e32 v0, 0
	global_load_dword v1, v0, s[10:11] sc1
	s_mov_b64 s[16:17], 0
	s_waitcnt vmcnt(0)
	v_cmp_lt_u32_e32 vcc, v1, v4
	s_andn2_b64 vcc, vcc, s[98:99]
	s_and_saveexec_b64 s[14:15], vcc
	s_cbranch_execz .LBB0_1241
	s_add_u32 s12, s28, 0x200
	s_addc_u32 s13, s29, 0
	s_mov_b32 s3, 1
	s_branch .LBB0_1234
